# combo: cvt full-line stores + decoupled, I8 epilogue row scales batched, P6 residual loads batched, barrier leader bumps generation before its acquire
# speedup vs baseline: 1.0153x; 1.0153x over previous
.LBB0_124:
	s_or_b64 exec, exec, s[10:11]
	s_mov_b64 s[10:11], exec
	v_mbcnt_lo_u32_b32 v1, s10, 0
	v_mbcnt_hi_u32_b32 v1, s11, v1
	v_cmp_eq_u32_e32 vcc, 0, v1
	s_waitcnt vmcnt(0)
	s_and_saveexec_b64 s[12:13], vcc
	s_cbranch_execz .LBB0_126
	s_bcnt1_i32_b64 s10, s[10:11]
	v_mov_b32_e32 v1, 0x2000
	v_mov_b32_e32 v2, s10
	global_atomic_add v1, v2, s[8:9] offset:1024
.LBB0_126:
	s_or_b64 exec, exec, s[12:13]
	buffer_inv sc1
	s_waitcnt vmcnt(0)

.LBB0_143:
	v_lshl_or_b32 v160, s6, 8, v183
	v_ashrrev_i32_e32 v161, 31, v160
	v_lshl_add_u64 v[46:47], v[160:161], 2, s[18:19]
	global_load_dwordx4 v[54:57], v[46:47], off offset:16
	global_load_dwordx4 v[58:61], v[46:47], off
	v_lshl_add_u32 v162, s30, 8, v181
	v_ashrrev_i32_e32 v163, 31, v162
	v_lshl_add_u64 v[164:165], v[162:163], 2, s[16:17]
	global_load_dword v166, v[164:165], off
	global_load_dwordx4 v[42:45], v[46:47], off offset:528
	s_nop 0
	global_load_dwordx4 v[46:49], v[46:47], off offset:512
	global_load_dword v192, v[164:165], off offset:64
	global_load_dword v193, v[164:165], off offset:128
	global_load_dword v194, v[164:165], off offset:192
	global_load_dword v195, v[164:165], off offset:512
	global_load_dword v196, v[164:165], off offset:576
	global_load_dword v197, v[164:165], off offset:640
	global_load_dword v198, v[164:165], off offset:704
	v_cvt_f32_i32_e32 v143, v143
	v_cvt_f32_i32_e32 v142, v142
	v_cvt_f32_i32_e32 v145, v145
	v_cvt_f32_i32_e32 v144, v144
	v_cvt_f32_i32_e32 v171, v139
	v_cvt_f32_i32_e32 v170, v138
	v_cvt_f32_i32_e32 v189, v141
	v_cvt_f32_i32_e32 v188, v140
	s_cmp_lt_i32 s6, 22
	v_mov_b64_e32 v[168:169], s[14:15]
	s_cselect_b64 s[30:31], -1, 0
	v_mad_i64_i32 v[138:139], s[34:35], v162, s64, v[168:169]
	s_mov_b64 s[6:7], -1
	v_lshl_add_u64 v[140:141], v[160:161], 1, v[138:139]
	s_and_b64 vcc, exec, s[30:31]
	s_waitcnt vmcnt(0)
	v_pk_mul_f32 v[188:189], v[56:57], v[188:189]
	v_pk_mul_f32 v[144:145], v[60:61], v[144:145]
	v_pk_mul_f32 v[142:143], v[58:59], v[142:143]
	v_pk_mul_f32 v[190:191], v[54:55], v[170:171]
	v_pk_mul_f32 v[170:171], v[142:143], v[166:167] op_sel_hi:[1,0]
	v_pk_mul_f32 v[168:169], v[144:145], v[166:167] op_sel_hi:[1,0]
	v_pk_mul_f32 v[144:145], v[190:191], v[166:167] op_sel_hi:[1,0]
	v_pk_mul_f32 v[142:143], v[188:189], v[166:167] op_sel_hi:[1,0]
	s_cbranch_vccz .LBB0_145
	v_cvt_pk_bf16_f32 v188, v170, v171
	v_cvt_pk_bf16_f32 v189, v168, v169
	v_cvt_pk_bf16_f32 v190, v144, v145
	v_cvt_pk_bf16_f32 v191, v142, v143
	global_store_dwordx4 v[140:141], v[188:191], off
	s_mov_b64 s[6:7], 0

.LBB0_151:
	v_or_b32_e32 v132, 16, v162
	v_ashrrev_i32_e32 v133, 31, v132
	v_lshl_add_u64 v[130:131], v[132:133], 2, s[16:17]
	v_mov_b32_e32 v130, v192
	v_cvt_f32_i32_e32 v127, v127
	v_cvt_f32_i32_e32 v126, v126
	v_cvt_f32_i32_e32 v129, v129
	v_cvt_f32_i32_e32 v128, v128
	v_cvt_f32_i32_e32 v137, v123
	v_cvt_f32_i32_e32 v136, v122
	v_cvt_f32_i32_e32 v139, v125
	v_cvt_f32_i32_e32 v138, v124
	v_mov_b64_e32 v[134:135], s[14:15]
	v_mad_i64_i32 v[122:123], s[30:31], v132, s64, v[134:135]
	v_pk_mul_f32 v[128:129], v[60:61], v[128:129]
	v_pk_mul_f32 v[126:127], v[58:59], v[126:127]
	v_pk_mul_f32 v[138:139], v[56:57], v[138:139]
	v_pk_mul_f32 v[136:137], v[54:55], v[136:137]
	s_and_b64 vcc, exec, s[6:7]
	v_lshl_add_u64 v[124:125], v[160:161], 1, v[122:123]
	s_mov_b64 s[30:31], -1
	v_pk_mul_f32 v[132:133], v[128:129], v[130:131] op_sel_hi:[1,0]
	v_pk_mul_f32 v[134:135], v[126:127], v[130:131] op_sel_hi:[1,0]
	v_pk_mul_f32 v[126:127], v[138:139], v[130:131] op_sel_hi:[1,0]
	v_pk_mul_f32 v[128:129], v[136:137], v[130:131] op_sel_hi:[1,0]
	s_cbranch_vccnz .LBB0_153
	s_mov_b64 s[30:31], 0
	v_cvt_pk_bf16_f32 v136, v134, v135
	v_cvt_pk_bf16_f32 v137, v132, v133
	v_cvt_pk_bf16_f32 v138, v128, v129
	v_cvt_pk_bf16_f32 v139, v126, v127
	global_store_dwordx4 v[124:125], v[136:139], off

.LBB0_159:
	v_or_b32_e32 v116, 32, v162
	v_ashrrev_i32_e32 v117, 31, v116
	v_lshl_add_u64 v[114:115], v[116:117], 2, s[16:17]
	v_mov_b32_e32 v114, v193
	v_cvt_f32_i32_e32 v111, v111
	v_cvt_f32_i32_e32 v110, v110
	v_cvt_f32_i32_e32 v113, v113
	v_cvt_f32_i32_e32 v112, v112
	v_cvt_f32_i32_e32 v121, v107
	v_cvt_f32_i32_e32 v120, v106
	v_cvt_f32_i32_e32 v123, v109
	v_cvt_f32_i32_e32 v122, v108
	v_mov_b64_e32 v[118:119], s[14:15]
	v_mad_i64_i32 v[106:107], s[30:31], v116, s64, v[118:119]
	v_pk_mul_f32 v[112:113], v[60:61], v[112:113]
	v_pk_mul_f32 v[110:111], v[58:59], v[110:111]
	v_pk_mul_f32 v[122:123], v[56:57], v[122:123]
	v_pk_mul_f32 v[120:121], v[54:55], v[120:121]
	s_and_b64 vcc, exec, s[6:7]
	v_lshl_add_u64 v[108:109], v[160:161], 1, v[106:107]
	s_mov_b64 s[30:31], -1
	v_pk_mul_f32 v[116:117], v[112:113], v[114:115] op_sel_hi:[1,0]
	v_pk_mul_f32 v[118:119], v[110:111], v[114:115] op_sel_hi:[1,0]
	v_pk_mul_f32 v[110:111], v[122:123], v[114:115] op_sel_hi:[1,0]
	v_pk_mul_f32 v[112:113], v[120:121], v[114:115] op_sel_hi:[1,0]
	s_cbranch_vccnz .LBB0_161
	s_mov_b64 s[30:31], 0
	v_cvt_pk_bf16_f32 v120, v118, v119
	v_cvt_pk_bf16_f32 v121, v116, v117
	v_cvt_pk_bf16_f32 v122, v112, v113
	v_cvt_pk_bf16_f32 v123, v110, v111
	global_store_dwordx4 v[108:109], v[120:123], off

.LBB0_167:
	v_or_b32_e32 v100, 48, v162
	v_ashrrev_i32_e32 v101, 31, v100
	v_lshl_add_u64 v[98:99], v[100:101], 2, s[16:17]
	v_mov_b32_e32 v98, v194
	v_cvt_f32_i32_e32 v95, v95
	v_cvt_f32_i32_e32 v94, v94
	v_cvt_f32_i32_e32 v97, v97
	v_cvt_f32_i32_e32 v96, v96
	v_cvt_f32_i32_e32 v105, v91
	v_cvt_f32_i32_e32 v104, v90
	v_cvt_f32_i32_e32 v107, v93
	v_cvt_f32_i32_e32 v106, v92
	v_mov_b64_e32 v[102:103], s[14:15]
	v_mad_i64_i32 v[90:91], s[30:31], v100, s64, v[102:103]
	v_pk_mul_f32 v[96:97], v[60:61], v[96:97]
	v_pk_mul_f32 v[94:95], v[58:59], v[94:95]
	v_pk_mul_f32 v[106:107], v[56:57], v[106:107]
	v_pk_mul_f32 v[104:105], v[54:55], v[104:105]
	s_and_b64 vcc, exec, s[6:7]
	v_lshl_add_u64 v[92:93], v[160:161], 1, v[90:91]
	s_mov_b64 s[30:31], -1
	v_pk_mul_f32 v[100:101], v[96:97], v[98:99] op_sel_hi:[1,0]
	v_pk_mul_f32 v[102:103], v[94:95], v[98:99] op_sel_hi:[1,0]
	v_pk_mul_f32 v[94:95], v[106:107], v[98:99] op_sel_hi:[1,0]
	v_pk_mul_f32 v[96:97], v[104:105], v[98:99] op_sel_hi:[1,0]
	s_cbranch_vccnz .LBB0_169
	s_mov_b64 s[30:31], 0
	v_cvt_pk_bf16_f32 v104, v102, v103
	v_cvt_pk_bf16_f32 v105, v100, v101
	v_cvt_pk_bf16_f32 v106, v96, v97
	v_cvt_pk_bf16_f32 v107, v94, v95
	global_store_dwordx4 v[92:93], v[104:107], off

.LBB0_175:
	v_mov_b32_e32 v82, v195
	v_cvt_f32_i32_e32 v79, v79
	v_cvt_f32_i32_e32 v78, v78
	v_cvt_f32_i32_e32 v81, v81
	v_cvt_f32_i32_e32 v80, v80
	v_cvt_f32_i32_e32 v87, v75
	v_cvt_f32_i32_e32 v86, v74
	v_cvt_f32_i32_e32 v89, v77
	v_cvt_f32_i32_e32 v88, v76
	v_add_u32_e32 v83, 0x80, v162
	v_mov_b64_e32 v[84:85], s[14:15]
	v_mad_i64_i32 v[74:75], s[30:31], v83, s64, v[84:85]
	v_pk_mul_f32 v[80:81], v[60:61], v[80:81]
	v_pk_mul_f32 v[78:79], v[58:59], v[78:79]
	v_pk_mul_f32 v[88:89], v[56:57], v[88:89]
	v_pk_mul_f32 v[90:91], v[54:55], v[86:87]
	s_and_b64 vcc, exec, s[6:7]
	v_lshl_add_u64 v[76:77], v[160:161], 1, v[74:75]
	s_mov_b64 s[30:31], -1
	v_pk_mul_f32 v[84:85], v[80:81], v[82:83] op_sel_hi:[1,0]
	v_pk_mul_f32 v[86:87], v[78:79], v[82:83] op_sel_hi:[1,0]
	v_pk_mul_f32 v[78:79], v[88:89], v[82:83] op_sel_hi:[1,0]
	v_pk_mul_f32 v[80:81], v[90:91], v[82:83] op_sel_hi:[1,0]
	s_cbranch_vccnz .LBB0_177
	s_mov_b64 s[30:31], 0
	v_cvt_pk_bf16_f32 v88, v86, v87
	v_cvt_pk_bf16_f32 v89, v84, v85
	v_cvt_pk_bf16_f32 v90, v80, v81
	v_cvt_pk_bf16_f32 v91, v78, v79
	global_store_dwordx4 v[76:77], v[88:91], off

.LBB0_183:
	v_mov_b32_e32 v66, v196
	v_cvt_f32_i32_e32 v63, v63
	v_cvt_f32_i32_e32 v62, v62
	v_cvt_f32_i32_e32 v65, v65
	v_cvt_f32_i32_e32 v64, v64
	v_cvt_f32_i32_e32 v71, v51
	v_cvt_f32_i32_e32 v70, v50
	v_cvt_f32_i32_e32 v73, v53
	v_cvt_f32_i32_e32 v72, v52
	v_add_u32_e32 v67, 0x90, v162
	v_mov_b64_e32 v[68:69], s[14:15]
	v_mad_i64_i32 v[50:51], s[30:31], v67, s64, v[68:69]
	v_pk_mul_f32 v[64:65], v[60:61], v[64:65]
	v_pk_mul_f32 v[62:63], v[58:59], v[62:63]
	v_pk_mul_f32 v[72:73], v[56:57], v[72:73]
	v_pk_mul_f32 v[74:75], v[54:55], v[70:71]
	s_and_b64 vcc, exec, s[6:7]
	v_lshl_add_u64 v[52:53], v[160:161], 1, v[50:51]
	s_mov_b64 s[30:31], -1
	v_pk_mul_f32 v[68:69], v[64:65], v[66:67] op_sel_hi:[1,0]
	v_pk_mul_f32 v[70:71], v[62:63], v[66:67] op_sel_hi:[1,0]
	v_pk_mul_f32 v[62:63], v[72:73], v[66:67] op_sel_hi:[1,0]
	v_pk_mul_f32 v[64:65], v[74:75], v[66:67] op_sel_hi:[1,0]
	s_cbranch_vccnz .LBB0_185
	s_mov_b64 s[30:31], 0
	v_cvt_pk_bf16_f32 v72, v70, v71
	v_cvt_pk_bf16_f32 v73, v68, v69
	v_cvt_pk_bf16_f32 v74, v64, v65
	v_cvt_pk_bf16_f32 v75, v62, v63
	global_store_dwordx4 v[52:53], v[72:75], off

.LBB0_191:
	v_mov_b32_e32 v34, v197
	v_cvt_f32_i32_e32 v31, v31
	v_cvt_f32_i32_e32 v30, v30
	v_cvt_f32_i32_e32 v33, v33
	v_cvt_f32_i32_e32 v32, v32
	v_cvt_f32_i32_e32 v39, v27
	v_cvt_f32_i32_e32 v38, v26
	v_cvt_f32_i32_e32 v41, v29
	v_cvt_f32_i32_e32 v40, v28
	v_add_u32_e32 v35, 0xa0, v162
	v_mov_b64_e32 v[36:37], s[14:15]
	v_mad_i64_i32 v[26:27], s[30:31], v35, s64, v[36:37]
	v_pk_mul_f32 v[32:33], v[60:61], v[32:33]
	v_pk_mul_f32 v[30:31], v[58:59], v[30:31]
	v_pk_mul_f32 v[40:41], v[56:57], v[40:41]
	v_pk_mul_f32 v[50:51], v[54:55], v[38:39]
	s_and_b64 vcc, exec, s[6:7]
	v_lshl_add_u64 v[28:29], v[160:161], 1, v[26:27]
	s_mov_b64 s[30:31], -1
	v_pk_mul_f32 v[36:37], v[32:33], v[34:35] op_sel_hi:[1,0]
	v_pk_mul_f32 v[38:39], v[30:31], v[34:35] op_sel_hi:[1,0]
	v_pk_mul_f32 v[30:31], v[40:41], v[34:35] op_sel_hi:[1,0]
	v_pk_mul_f32 v[32:33], v[50:51], v[34:35] op_sel_hi:[1,0]
	s_cbranch_vccnz .LBB0_193
	s_mov_b64 s[30:31], 0
	v_cvt_pk_bf16_f32 v50, v38, v39
	v_cvt_pk_bf16_f32 v51, v36, v37
	v_cvt_pk_bf16_f32 v52, v32, v33
	v_cvt_pk_bf16_f32 v53, v30, v31
	global_store_dwordx4 v[28:29], v[50:53], off

.LBB0_199:
	v_mov_b32_e32 v18, v198
	v_cvt_f32_i32_e32 v15, v15
	v_cvt_f32_i32_e32 v14, v14
	v_cvt_f32_i32_e32 v17, v17
	v_cvt_f32_i32_e32 v16, v16
	v_cvt_f32_i32_e32 v23, v11
	v_cvt_f32_i32_e32 v22, v10
	v_cvt_f32_i32_e32 v25, v13
	v_cvt_f32_i32_e32 v24, v12
	v_add_u32_e32 v19, 0xb0, v162
	v_mov_b64_e32 v[20:21], s[14:15]
	v_mad_i64_i32 v[10:11], s[30:31], v19, s64, v[20:21]
	v_pk_mul_f32 v[16:17], v[60:61], v[16:17]
	v_pk_mul_f32 v[14:15], v[58:59], v[14:15]
	v_pk_mul_f32 v[24:25], v[56:57], v[24:25]
	v_pk_mul_f32 v[26:27], v[54:55], v[22:23]
	s_and_b64 vcc, exec, s[6:7]
	v_lshl_add_u64 v[12:13], v[160:161], 1, v[10:11]
	s_mov_b64 s[30:31], -1
	v_pk_mul_f32 v[20:21], v[16:17], v[18:19] op_sel_hi:[1,0]
	v_pk_mul_f32 v[22:23], v[14:15], v[18:19] op_sel_hi:[1,0]
	v_pk_mul_f32 v[14:15], v[24:25], v[18:19] op_sel_hi:[1,0]
	v_pk_mul_f32 v[16:17], v[26:27], v[18:19] op_sel_hi:[1,0]
	s_cbranch_vccnz .LBB0_201
	s_mov_b64 s[30:31], 0
	v_cvt_pk_bf16_f32 v24, v22, v23
	v_cvt_pk_bf16_f32 v25, v20, v21
	v_cvt_pk_bf16_f32 v26, v16, v17
	v_cvt_pk_bf16_f32 v27, v14, v15
	global_store_dwordx4 v[12:13], v[24:27], off

.LBB0_310:
	v_lshl_or_b32 v160, s6, 8, v175
	v_ashrrev_i32_e32 v161, 31, v160
	v_lshl_add_u64 v[46:47], v[160:161], 2, s[18:19]
	global_load_dwordx4 v[54:57], v[46:47], off offset:16
	global_load_dwordx4 v[58:61], v[46:47], off
	v_lshl_add_u32 v162, s30, 8, v179
	v_ashrrev_i32_e32 v163, 31, v162
	v_lshl_add_u64 v[164:165], v[162:163], 2, s[16:17]
	global_load_dword v166, v[164:165], off
	global_load_dwordx4 v[42:45], v[46:47], off offset:528
	s_nop 0
	global_load_dwordx4 v[46:49], v[46:47], off offset:512
	global_load_dword v192, v[164:165], off offset:64
	global_load_dword v193, v[164:165], off offset:128
	global_load_dword v194, v[164:165], off offset:192
	global_load_dword v195, v[164:165], off offset:512
	global_load_dword v196, v[164:165], off offset:576
	global_load_dword v197, v[164:165], off offset:640
	global_load_dword v198, v[164:165], off offset:704
	v_cvt_f32_i32_e32 v143, v143
	v_cvt_f32_i32_e32 v142, v142
	v_cvt_f32_i32_e32 v145, v145
	v_cvt_f32_i32_e32 v144, v144
	v_cvt_f32_i32_e32 v171, v139
	v_cvt_f32_i32_e32 v170, v138
	v_cvt_f32_i32_e32 v181, v141
	v_cvt_f32_i32_e32 v180, v140
	s_cmp_lt_i32 s6, 22
	v_mov_b64_e32 v[168:169], s[14:15]
	s_cselect_b64 s[30:31], -1, 0
	v_mad_i64_i32 v[138:139], s[34:35], v162, s64, v[168:169]
	s_mov_b64 s[6:7], -1
	v_lshl_add_u64 v[140:141], v[160:161], 1, v[138:139]
	s_and_b64 vcc, exec, s[30:31]
	s_waitcnt vmcnt(0)
	v_pk_mul_f32 v[180:181], v[56:57], v[180:181]
	v_pk_mul_f32 v[144:145], v[60:61], v[144:145]
	v_pk_mul_f32 v[142:143], v[58:59], v[142:143]
	v_pk_mul_f32 v[182:183], v[54:55], v[170:171]
	v_pk_mul_f32 v[170:171], v[142:143], v[166:167] op_sel_hi:[1,0]
	v_pk_mul_f32 v[168:169], v[144:145], v[166:167] op_sel_hi:[1,0]
	v_pk_mul_f32 v[144:145], v[182:183], v[166:167] op_sel_hi:[1,0]
	v_pk_mul_f32 v[142:143], v[180:181], v[166:167] op_sel_hi:[1,0]
	s_cbranch_vccz .LBB0_312
	v_cvt_pk_bf16_f32 v180, v170, v171
	v_cvt_pk_bf16_f32 v181, v168, v169
	v_cvt_pk_bf16_f32 v182, v144, v145
	v_cvt_pk_bf16_f32 v183, v142, v143
	global_store_dwordx4 v[140:141], v[180:183], off
	s_mov_b64 s[6:7], 0

.LBB0_846:
	v_lshl_add_u32 v150, s36, 8, v1
	v_lshl_or_b32 v148, s65, 8, v153
	v_ashrrev_i32_e32 v151, 31, v150
	v_ashrrev_i32_e32 v149, 31, v148
	v_lshlrev_b64 v[146:147], 11, v[150:151]
	v_lshl_add_u64 v[146:147], v[146:147], 0, v[148:149]
	v_lshlrev_b64 v[146:147], 1, v[146:147]
	v_lshl_add_u64 v[162:163], s[12:13], 0, v[146:147]
	s_mov_b64 s[80:81], s[12:13]
	global_load_dwordx4 v[170:173], v146, s[80:81]
	global_load_dwordx4 v[174:177], v146, s[80:81] offset:256
	s_add_u32 s80, s12, 0x10000
	s_addc_u32 s81, s13, 0
	global_load_dwordx4 v[178:181], v146, s[80:81]
	global_load_dwordx4 v[182:185], v146, s[80:81] offset:256
	s_add_u32 s80, s12, 0x20000
	s_addc_u32 s81, s13, 0
	global_load_dwordx4 v[186:189], v146, s[80:81]
	global_load_dwordx4 v[190:193], v146, s[80:81] offset:256
	s_add_u32 s80, s12, 0x30000
	s_addc_u32 s81, s13, 0
	global_load_dwordx4 v[194:197], v146, s[80:81]
	global_load_dwordx4 v[198:201], v146, s[80:81] offset:256
	s_add_u32 s80, s12, 0x80000
	s_addc_u32 s81, s13, 0
	global_load_dwordx4 v[202:205], v146, s[80:81]
	global_load_dwordx4 v[206:209], v146, s[80:81] offset:256
	s_add_u32 s80, s12, 0x90000
	s_addc_u32 s81, s13, 0
	global_load_dwordx4 v[210:213], v146, s[80:81]
	global_load_dwordx4 v[214:217], v146, s[80:81] offset:256
	s_add_u32 s80, s12, 0xa0000
	s_addc_u32 s81, s13, 0
	global_load_dwordx4 v[228:231], v146, s[80:81]
	global_load_dwordx4 v[232:235], v146, s[80:81] offset:256
	s_add_u32 s80, s12, 0xb0000
	s_addc_u32 s81, s13, 0
	global_load_dwordx4 v[236:239], v146, s[80:81]
	global_load_dwordx4 v[240:243], v146, s[80:81] offset:256
	s_waitcnt vmcnt(15)
	s_nop 1
	v_mov_b32_e32 v158, v170
	v_mov_b32_e32 v159, v171
	v_mov_b32_e32 v160, v172
	v_mov_b32_e32 v161, v173
	s_andn2_b64 vcc, exec, s[4:5]
	s_mov_b64 s[4:5], -1
	s_nop 1
	v_lshlrev_b32_e32 v164, 16, v158
	v_and_b32_e32 v165, 0xffff0000, v158
	v_lshlrev_b32_e32 v158, 16, v159
	v_and_b32_e32 v159, 0xffff0000, v159
	v_lshlrev_b32_e32 v166, 16, v160
	v_and_b32_e32 v167, 0xffff0000, v160
	v_lshlrev_b32_e32 v160, 16, v161
	v_and_b32_e32 v161, 0xffff0000, v161
	v_pk_add_f32 v[128:129], v[128:129], v[158:159]
	v_pk_add_f32 v[126:127], v[126:127], v[164:165]
	v_pk_add_f32 v[158:159], v[124:125], v[160:161]
	v_pk_add_f32 v[124:125], v[122:123], v[166:167]
	v_cvt_pk_bf16_f32 v122, v126, v127
	v_cvt_pk_bf16_f32 v123, v128, v129
	v_lshl_add_u64 v[160:161], s[14:15], 0, v[146:147]
	v_cvt_pk_bf16_f32 v124, v124, v125
	v_cvt_pk_bf16_f32 v125, v158, v159
	s_waitcnt vmcnt(14)
	s_nop 1
	v_mov_b32_e32 v126, v174
	v_mov_b32_e32 v127, v175
	v_mov_b32_e32 v128, v176
	v_mov_b32_e32 v129, v177
	v_or_b32_e32 v158, 16, v150
	v_ashrrev_i32_e32 v159, 31, v158
	v_lshlrev_b64 v[158:159], 11, v[158:159]
	v_lshl_add_u64 v[158:159], v[158:159], 0, v[148:149]
	global_store_dwordx4 v[160:161], v[122:125], off
	v_lshlrev_b64 v[158:159], 1, v[158:159]
	v_lshl_add_u64 v[162:163], s[12:13], 0, v[158:159]
	s_nop 1
	v_lshlrev_b32_e32 v122, 16, v126
	v_and_b32_e32 v123, 0xffff0000, v126
	v_lshlrev_b32_e32 v124, 16, v127
	v_and_b32_e32 v125, 0xffff0000, v127
	v_lshlrev_b32_e32 v126, 16, v128
	v_and_b32_e32 v127, 0xffff0000, v128
	v_lshlrev_b32_e32 v128, 16, v129
	v_and_b32_e32 v129, 0xffff0000, v129
	v_pk_add_f32 v[114:115], v[114:115], v[122:123]
	v_pk_add_f32 v[122:123], v[112:113], v[128:129]
	v_pk_add_f32 v[112:113], v[110:111], v[126:127]
	v_pk_add_f32 v[116:117], v[116:117], v[124:125]
	v_cvt_pk_bf16_f32 v110, v114, v115
	s_nop 0
	v_cvt_pk_bf16_f32 v111, v116, v117
	v_cvt_pk_bf16_f32 v112, v112, v113
	v_cvt_pk_bf16_f32 v113, v122, v123
	global_store_dwordx4 v[160:161], v[110:113], off offset:256
	s_waitcnt vmcnt(15)
	s_nop 1
	v_mov_b32_e32 v110, v178
	v_mov_b32_e32 v111, v179
	v_mov_b32_e32 v112, v180
	v_mov_b32_e32 v113, v181
	s_nop 1
	v_lshlrev_b32_e32 v114, 16, v110
	v_and_b32_e32 v115, 0xffff0000, v110
	v_lshlrev_b32_e32 v110, 16, v111
	v_and_b32_e32 v111, 0xffff0000, v111
	v_lshlrev_b32_e32 v116, 16, v112
	v_and_b32_e32 v117, 0xffff0000, v112
	v_lshlrev_b32_e32 v112, 16, v113
	v_and_b32_e32 v113, 0xffff0000, v113
	v_pk_add_f32 v[110:111], v[120:121], v[110:111]
	v_pk_add_f32 v[112:113], v[108:109], v[112:113]
	v_pk_add_f32 v[108:109], v[106:107], v[116:117]
	v_pk_add_f32 v[114:115], v[118:119], v[114:115]
	v_lshl_add_u64 v[116:117], s[14:15], 0, v[158:159]
	v_cvt_pk_bf16_f32 v106, v114, v115
	v_cvt_pk_bf16_f32 v107, v110, v111
	v_cvt_pk_bf16_f32 v108, v108, v109
	v_cvt_pk_bf16_f32 v109, v112, v113
	s_waitcnt vmcnt(14)
	s_nop 1
	v_mov_b32_e32 v110, v182
	v_mov_b32_e32 v111, v183
	v_mov_b32_e32 v112, v184
	v_mov_b32_e32 v113, v185
	v_or_b32_e32 v114, 32, v150
	v_ashrrev_i32_e32 v115, 31, v114
	v_lshlrev_b64 v[114:115], 11, v[114:115]
	v_lshl_add_u64 v[114:115], v[114:115], 0, v[148:149]
	global_store_dwordx4 v[116:117], v[106:109], off
	v_lshlrev_b64 v[114:115], 1, v[114:115]
	v_lshl_add_u64 v[118:119], s[12:13], 0, v[114:115]
	s_nop 1
	v_lshlrev_b32_e32 v106, 16, v110
	v_and_b32_e32 v107, 0xffff0000, v110
	v_lshlrev_b32_e32 v108, 16, v111
	v_and_b32_e32 v109, 0xffff0000, v111
	v_lshlrev_b32_e32 v110, 16, v112
	v_and_b32_e32 v111, 0xffff0000, v112
	v_lshlrev_b32_e32 v112, 16, v113
	v_and_b32_e32 v113, 0xffff0000, v113
	v_pk_add_f32 v[98:99], v[98:99], v[106:107]
	v_pk_add_f32 v[106:107], v[96:97], v[112:113]
	v_pk_add_f32 v[96:97], v[94:95], v[110:111]
	v_pk_add_f32 v[100:101], v[100:101], v[108:109]
	v_cvt_pk_bf16_f32 v94, v98, v99
	s_nop 0
	v_cvt_pk_bf16_f32 v95, v100, v101
	v_cvt_pk_bf16_f32 v96, v96, v97
	v_cvt_pk_bf16_f32 v97, v106, v107
	global_store_dwordx4 v[116:117], v[94:97], off offset:256
	s_waitcnt vmcnt(15)
	s_nop 1
	v_mov_b32_e32 v94, v186
	v_mov_b32_e32 v95, v187
	v_mov_b32_e32 v96, v188
	v_mov_b32_e32 v97, v189
	s_nop 1
	v_lshlrev_b32_e32 v98, 16, v94
	v_and_b32_e32 v99, 0xffff0000, v94
	v_lshlrev_b32_e32 v94, 16, v95
	v_and_b32_e32 v95, 0xffff0000, v95
	v_lshlrev_b32_e32 v100, 16, v96
	v_and_b32_e32 v101, 0xffff0000, v96
	v_lshlrev_b32_e32 v96, 16, v97
	v_and_b32_e32 v97, 0xffff0000, v97
	v_pk_add_f32 v[94:95], v[104:105], v[94:95]
	v_pk_add_f32 v[96:97], v[92:93], v[96:97]
	v_pk_add_f32 v[92:93], v[90:91], v[100:101]
	v_pk_add_f32 v[98:99], v[102:103], v[98:99]
	v_lshl_add_u64 v[100:101], s[14:15], 0, v[114:115]
	v_cvt_pk_bf16_f32 v90, v98, v99
	v_cvt_pk_bf16_f32 v91, v94, v95
	v_cvt_pk_bf16_f32 v92, v92, v93
	v_cvt_pk_bf16_f32 v93, v96, v97
	s_waitcnt vmcnt(14)
	s_nop 1
	v_mov_b32_e32 v94, v190
	v_mov_b32_e32 v95, v191
	v_mov_b32_e32 v96, v192
	v_mov_b32_e32 v97, v193
	v_or_b32_e32 v98, 48, v150
	v_ashrrev_i32_e32 v99, 31, v98
	v_lshlrev_b64 v[98:99], 11, v[98:99]
	v_lshl_add_u64 v[98:99], v[98:99], 0, v[148:149]
	global_store_dwordx4 v[100:101], v[90:93], off
	v_lshlrev_b64 v[98:99], 1, v[98:99]
	v_lshl_add_u64 v[102:103], s[12:13], 0, v[98:99]
	s_nop 1
	v_lshlrev_b32_e32 v90, 16, v94
	v_and_b32_e32 v91, 0xffff0000, v94
	v_lshlrev_b32_e32 v92, 16, v95
	v_and_b32_e32 v93, 0xffff0000, v95
	v_lshlrev_b32_e32 v94, 16, v96
	v_and_b32_e32 v95, 0xffff0000, v96
	v_lshlrev_b32_e32 v96, 16, v97
	v_and_b32_e32 v97, 0xffff0000, v97
	v_pk_add_f32 v[82:83], v[82:83], v[90:91]
	v_pk_add_f32 v[90:91], v[80:81], v[96:97]
	v_pk_add_f32 v[80:81], v[78:79], v[94:95]
	v_pk_add_f32 v[84:85], v[84:85], v[92:93]
	v_cvt_pk_bf16_f32 v78, v82, v83
	s_nop 0
	v_cvt_pk_bf16_f32 v79, v84, v85
	v_cvt_pk_bf16_f32 v80, v80, v81
	v_cvt_pk_bf16_f32 v81, v90, v91
	global_store_dwordx4 v[100:101], v[78:81], off offset:256
	s_waitcnt vmcnt(15)
	s_nop 1
	v_mov_b32_e32 v78, v194
	v_mov_b32_e32 v79, v195
	v_mov_b32_e32 v80, v196
	v_mov_b32_e32 v81, v197
	s_nop 1
	v_lshlrev_b32_e32 v82, 16, v78
	v_and_b32_e32 v83, 0xffff0000, v78
	v_lshlrev_b32_e32 v78, 16, v79
	v_and_b32_e32 v79, 0xffff0000, v79
	v_lshlrev_b32_e32 v84, 16, v80
	v_and_b32_e32 v85, 0xffff0000, v80
	v_lshlrev_b32_e32 v80, 16, v81
	v_and_b32_e32 v81, 0xffff0000, v81
	v_pk_add_f32 v[78:79], v[88:89], v[78:79]
	v_pk_add_f32 v[80:81], v[76:77], v[80:81]
	v_pk_add_f32 v[76:77], v[74:75], v[84:85]
	v_pk_add_f32 v[82:83], v[86:87], v[82:83]
	v_lshl_add_u64 v[84:85], s[14:15], 0, v[98:99]
	v_cvt_pk_bf16_f32 v74, v82, v83
	v_cvt_pk_bf16_f32 v75, v78, v79
	v_cvt_pk_bf16_f32 v76, v76, v77
	v_cvt_pk_bf16_f32 v77, v80, v81
	s_waitcnt vmcnt(14)
	s_nop 1
	v_mov_b32_e32 v78, v198
	v_mov_b32_e32 v79, v199
	v_mov_b32_e32 v80, v200
	v_mov_b32_e32 v81, v201
	v_lshl_add_u64 v[82:83], v[146:147], 0, s[8:9]
	global_store_dwordx4 v[84:85], v[74:77], off
	v_lshl_add_u64 v[86:87], s[12:13], 0, v[82:83]
	s_nop 1
	v_lshlrev_b32_e32 v74, 16, v78
	v_and_b32_e32 v75, 0xffff0000, v78
	v_lshlrev_b32_e32 v76, 16, v79
	v_and_b32_e32 v77, 0xffff0000, v79
	v_lshlrev_b32_e32 v78, 16, v80
	v_and_b32_e32 v79, 0xffff0000, v80
	v_lshlrev_b32_e32 v80, 16, v81
	v_and_b32_e32 v81, 0xffff0000, v81
	v_pk_add_f32 v[70:71], v[70:71], v[74:75]
	v_pk_add_f32 v[74:75], v[68:69], v[80:81]
	v_pk_add_f32 v[68:69], v[66:67], v[78:79]
	v_pk_add_f32 v[72:73], v[72:73], v[76:77]
	v_cvt_pk_bf16_f32 v66, v70, v71
	s_nop 0
	v_cvt_pk_bf16_f32 v67, v72, v73
	v_cvt_pk_bf16_f32 v68, v68, v69
	v_cvt_pk_bf16_f32 v69, v74, v75
	global_store_dwordx4 v[84:85], v[66:69], off offset:256
	s_waitcnt vmcnt(15)
	s_nop 1
	v_mov_b32_e32 v66, v202
	v_mov_b32_e32 v67, v203
	v_mov_b32_e32 v68, v204
	v_mov_b32_e32 v69, v205
	s_nop 1
	v_lshlrev_b32_e32 v70, 16, v66
	v_and_b32_e32 v71, 0xffff0000, v66
	v_lshlrev_b32_e32 v66, 16, v67
	v_and_b32_e32 v67, 0xffff0000, v67
	v_lshlrev_b32_e32 v72, 16, v68
	v_and_b32_e32 v73, 0xffff0000, v68
	v_lshlrev_b32_e32 v68, 16, v69
	v_and_b32_e32 v69, 0xffff0000, v69
	v_pk_add_f32 v[64:65], v[64:65], v[66:67]
	v_pk_add_f32 v[62:63], v[62:63], v[70:71]
	v_pk_add_f32 v[66:67], v[60:61], v[68:69]
	v_pk_add_f32 v[60:61], v[58:59], v[72:73]
	v_cvt_pk_bf16_f32 v58, v62, v63
	v_cvt_pk_bf16_f32 v59, v64, v65
	v_lshl_add_u64 v[68:69], s[14:15], 0, v[82:83]
	v_cvt_pk_bf16_f32 v60, v60, v61
	v_cvt_pk_bf16_f32 v61, v66, v67
	s_waitcnt vmcnt(14)
	s_nop 1
	v_mov_b32_e32 v62, v206
	v_mov_b32_e32 v63, v207
	v_mov_b32_e32 v64, v208
	v_mov_b32_e32 v65, v209
	v_lshl_add_u64 v[66:67], v[146:147], 0, s[20:21]
	global_store_dwordx4 v[68:69], v[58:61], off
	v_lshl_add_u64 v[70:71], s[12:13], 0, v[66:67]
	s_nop 1
	v_lshlrev_b32_e32 v58, 16, v62
	v_and_b32_e32 v59, 0xffff0000, v62
	v_lshlrev_b32_e32 v60, 16, v63
	v_and_b32_e32 v61, 0xffff0000, v63
	v_lshlrev_b32_e32 v62, 16, v64
	v_and_b32_e32 v63, 0xffff0000, v64
	v_lshlrev_b32_e32 v64, 16, v65
	v_and_b32_e32 v65, 0xffff0000, v65
	v_pk_add_f32 v[50:51], v[50:51], v[58:59]
	v_pk_add_f32 v[58:59], v[48:49], v[64:65]
	v_pk_add_f32 v[48:49], v[46:47], v[62:63]
	v_pk_add_f32 v[52:53], v[52:53], v[60:61]
	v_cvt_pk_bf16_f32 v46, v50, v51
	s_nop 0
	v_cvt_pk_bf16_f32 v47, v52, v53
	v_cvt_pk_bf16_f32 v48, v48, v49
	v_cvt_pk_bf16_f32 v49, v58, v59
	global_store_dwordx4 v[68:69], v[46:49], off offset:256
	s_waitcnt vmcnt(15)
	s_nop 1
	v_mov_b32_e32 v46, v210
	v_mov_b32_e32 v47, v211
	v_mov_b32_e32 v48, v212
	v_mov_b32_e32 v49, v213
	s_nop 1
	v_lshlrev_b32_e32 v50, 16, v46
	v_and_b32_e32 v51, 0xffff0000, v46
	v_lshlrev_b32_e32 v46, 16, v47
	v_and_b32_e32 v47, 0xffff0000, v47
	v_lshlrev_b32_e32 v52, 16, v48
	v_and_b32_e32 v53, 0xffff0000, v48
	v_lshlrev_b32_e32 v48, 16, v49
	v_and_b32_e32 v49, 0xffff0000, v49
	v_pk_add_f32 v[46:47], v[56:57], v[46:47]
	v_pk_add_f32 v[48:49], v[44:45], v[48:49]
	v_pk_add_f32 v[44:45], v[42:43], v[52:53]
	v_pk_add_f32 v[50:51], v[54:55], v[50:51]
	v_lshl_add_u64 v[52:53], s[14:15], 0, v[66:67]
	v_cvt_pk_bf16_f32 v42, v50, v51
	v_cvt_pk_bf16_f32 v43, v46, v47
	v_cvt_pk_bf16_f32 v44, v44, v45
	v_cvt_pk_bf16_f32 v45, v48, v49
	s_waitcnt vmcnt(14)
	s_nop 1
	v_mov_b32_e32 v46, v214
	v_mov_b32_e32 v47, v215
	v_mov_b32_e32 v48, v216
	v_mov_b32_e32 v49, v217
	v_lshl_add_u64 v[50:51], v[146:147], 0, s[22:23]
	global_store_dwordx4 v[52:53], v[42:45], off
	v_lshl_add_u64 v[54:55], s[12:13], 0, v[50:51]
	s_nop 1
	v_lshlrev_b32_e32 v42, 16, v46
	v_and_b32_e32 v43, 0xffff0000, v46
	v_lshlrev_b32_e32 v44, 16, v47
	v_and_b32_e32 v45, 0xffff0000, v47
	v_lshlrev_b32_e32 v46, 16, v48
	v_and_b32_e32 v47, 0xffff0000, v48
	v_lshlrev_b32_e32 v48, 16, v49
	v_and_b32_e32 v49, 0xffff0000, v49
	v_pk_add_f32 v[34:35], v[34:35], v[42:43]
	v_pk_add_f32 v[42:43], v[32:33], v[48:49]
	v_pk_add_f32 v[32:33], v[30:31], v[46:47]
	v_pk_add_f32 v[36:37], v[36:37], v[44:45]
	v_cvt_pk_bf16_f32 v30, v34, v35
	s_nop 0
	v_cvt_pk_bf16_f32 v31, v36, v37
	v_cvt_pk_bf16_f32 v32, v32, v33
	v_cvt_pk_bf16_f32 v33, v42, v43
	global_store_dwordx4 v[52:53], v[30:33], off offset:256
	s_waitcnt vmcnt(15)
	s_nop 1
	v_mov_b32_e32 v30, v228
	v_mov_b32_e32 v31, v229
	v_mov_b32_e32 v32, v230
	v_mov_b32_e32 v33, v231
	s_nop 1
	v_lshlrev_b32_e32 v34, 16, v30
	v_and_b32_e32 v35, 0xffff0000, v30
	v_lshlrev_b32_e32 v30, 16, v31
	v_and_b32_e32 v31, 0xffff0000, v31
	v_lshlrev_b32_e32 v36, 16, v32
	v_and_b32_e32 v37, 0xffff0000, v32
	v_lshlrev_b32_e32 v32, 16, v33
	v_and_b32_e32 v33, 0xffff0000, v33
	v_pk_add_f32 v[30:31], v[40:41], v[30:31]
	v_pk_add_f32 v[32:33], v[28:29], v[32:33]
	v_pk_add_f32 v[28:29], v[26:27], v[36:37]
	v_pk_add_f32 v[34:35], v[38:39], v[34:35]
	v_lshl_add_u64 v[36:37], s[14:15], 0, v[50:51]
	v_cvt_pk_bf16_f32 v26, v34, v35
	v_cvt_pk_bf16_f32 v27, v30, v31
	v_cvt_pk_bf16_f32 v28, v28, v29
	v_cvt_pk_bf16_f32 v29, v32, v33
	s_waitcnt vmcnt(14)
	s_nop 1
	v_mov_b32_e32 v30, v232
	v_mov_b32_e32 v31, v233
	v_mov_b32_e32 v32, v234
	v_mov_b32_e32 v33, v235
	v_lshl_add_u64 v[34:35], v[146:147], 0, s[24:25]
	global_store_dwordx4 v[36:37], v[26:29], off
	v_lshl_add_u64 v[38:39], s[12:13], 0, v[34:35]
	s_nop 1
	v_lshlrev_b32_e32 v26, 16, v30
	v_and_b32_e32 v27, 0xffff0000, v30
	v_lshlrev_b32_e32 v28, 16, v31
	v_and_b32_e32 v29, 0xffff0000, v31
	v_lshlrev_b32_e32 v30, 16, v32
	v_and_b32_e32 v31, 0xffff0000, v32
	v_lshlrev_b32_e32 v32, 16, v33
	v_and_b32_e32 v33, 0xffff0000, v33
	v_pk_add_f32 v[18:19], v[18:19], v[26:27]
	v_pk_add_f32 v[26:27], v[16:17], v[32:33]
	v_pk_add_f32 v[16:17], v[14:15], v[30:31]
	v_pk_add_f32 v[20:21], v[20:21], v[28:29]
	v_cvt_pk_bf16_f32 v14, v18, v19
	s_nop 0
	v_cvt_pk_bf16_f32 v15, v20, v21
	v_cvt_pk_bf16_f32 v16, v16, v17
	v_cvt_pk_bf16_f32 v17, v26, v27
	global_store_dwordx4 v[36:37], v[14:17], off offset:256
	s_waitcnt vmcnt(15)
	s_nop 1
	v_mov_b32_e32 v14, v236
	v_mov_b32_e32 v15, v237
	v_mov_b32_e32 v16, v238
	v_mov_b32_e32 v17, v239
	s_nop 1
	v_lshlrev_b32_e32 v18, 16, v14
	v_and_b32_e32 v19, 0xffff0000, v14
	v_lshlrev_b32_e32 v14, 16, v15
	v_and_b32_e32 v15, 0xffff0000, v15
	v_lshlrev_b32_e32 v20, 16, v16
	v_and_b32_e32 v21, 0xffff0000, v16
	v_lshlrev_b32_e32 v16, 16, v17
	v_and_b32_e32 v17, 0xffff0000, v17
	v_pk_add_f32 v[14:15], v[24:25], v[14:15]
	v_pk_add_f32 v[16:17], v[12:13], v[16:17]
	v_pk_add_f32 v[12:13], v[10:11], v[20:21]
	v_pk_add_f32 v[18:19], v[22:23], v[18:19]
	s_nop 0
	v_cvt_pk_bf16_f32 v10, v18, v19
	v_cvt_pk_bf16_f32 v11, v14, v15
	v_cvt_pk_bf16_f32 v12, v12, v13
	v_cvt_pk_bf16_f32 v13, v16, v17
	s_waitcnt vmcnt(14)
	s_nop 1
	v_mov_b32_e32 v14, v240
	v_mov_b32_e32 v15, v241
	v_mov_b32_e32 v16, v242
	v_mov_b32_e32 v17, v243
	v_lshl_add_u64 v[18:19], s[14:15], 0, v[34:35]
	global_store_dwordx4 v[18:19], v[10:13], off
	s_nop 1
	s_nop 0
	v_lshlrev_b32_e32 v10, 16, v14
	v_and_b32_e32 v11, 0xffff0000, v14
	v_lshlrev_b32_e32 v12, 16, v15
	v_and_b32_e32 v13, 0xffff0000, v15
	v_lshlrev_b32_e32 v14, 16, v16
	v_and_b32_e32 v15, 0xffff0000, v16
	v_lshlrev_b32_e32 v16, 16, v17
	v_and_b32_e32 v17, 0xffff0000, v17
	v_pk_add_f32 v[6:7], v[6:7], v[10:11]
	v_pk_add_f32 v[10:11], v[4:5], v[16:17]
	v_pk_add_f32 v[4:5], v[2:3], v[14:15]
	v_pk_add_f32 v[8:9], v[8:9], v[12:13]
	v_cvt_pk_bf16_f32 v2, v6, v7
	s_nop 0
	v_cvt_pk_bf16_f32 v3, v8, v9
	v_cvt_pk_bf16_f32 v4, v4, v5
	v_cvt_pk_bf16_f32 v5, v10, v11
	global_store_dwordx4 v[18:19], v[2:5], off offset:256
	s_cbranch_vccnz .LBB0_835
	s_andn2_b64 vcc, exec, s[10:11]
	s_cbranch_vccnz .LBB0_834
	s_barrier
	s_branch .LBB0_834
